# baseline (speedup 1.0000x reference)
_Z11gram_kernelPKfPKiS0_S0_S0_S0_S0_S0_S0_S0_S0_Pf:
	s_load_dwordx4 s[24:27], s[0:1], 0x0
	s_load_dwordx2 s[28:29], s[0:1], 0x40
	s_load_dwordx4 s[20:23], s[0:1], 0x30
	s_load_dwordx2 s[10:11], s[0:1], 0x58
	s_load_dwordx2 s[44:45], s[0:1], 0x20
	s_load_dwordx2 s[68:69], s[0:1], 0x10
	s_ashr_i32 s30, s2, 1
	s_getpc_b64 s[4:5]
	s_and_b32 s4, s4, 0xfffffc00
	v_lshlrev_b32_e32 v10, 7, v0
	v_mov_b32_e32 v11, 0
	s_ashr_i32 s31, s30, 31
	v_lshl_add_u64 v[2:3], s[4:5], 0, v[10:11]
	s_lshl_b64 s[4:5], s[30:31], 14
	s_waitcnt lgkmcnt(0)
	s_add_u32 s48, s20, s4
	s_addc_u32 s49, s21, s5
	s_movk_i32 s4, 0xa000
	s_movk_i32 s3, 0xbf
	v_lshl_add_u64 v[4:5], s[48:49], 0, v[10:11]
	s_mov_b32 s5, -1
	v_lshl_add_u64 v[4:5], v[4:5], 0, s[4:5]
	v_cmp_lt_u32_e32 vcc, s3, v0
	s_movk_i32 s3, 0x13f
	s_mov_b64 s[36:37], s[24:25]
	v_cndmask_b32_e32 v3, v3, v5, vcc
	v_cndmask_b32_e32 v2, v2, v4, vcc
	v_cmp_lt_u32_e32 vcc, s3, v0
	s_and_saveexec_b64 s[4:5], vcc
	s_cbranch_execz .LBB0_2
	v_and_b32_e32 v1, 16, v0
	v_mov_b32_e32 v2, s29
	v_mov_b32_e32 v3, s23
	v_cmp_eq_u32_e32 vcc, 0, v1
	s_lshl_b32 s3, s2, 1
	v_mov_b32_e32 v1, s28
	v_cndmask_b32_e32 v3, v2, v3, vcc
	v_mov_b32_e32 v2, s22
	s_and_b32 s3, s3, 0x1f0
	v_cndmask_b32_e32 v2, v1, v2, vcc
	v_and_or_b32 v1, v0, 15, s3
	v_lshlrev_b32_e32 v4, 7, v1
	v_mov_b32_e32 v5, 0
	v_lshl_add_u64 v[2:3], v[2:3], 0, v[4:5]
.LBB0_2:
	s_or_b64 exec, exec, s[4:5]
	s_movk_i32 s3, 0x160
	v_cmp_gt_u32_e32 vcc, s3, v0
	s_and_saveexec_b64 s[4:5], vcc
	s_cbranch_execz .LBB0_4
	global_load_dword v11, v[2:3], off
.LBB0_4:
	s_or_b64 exec, exec, s[4:5]
	s_lshl_b32 s46, s30, 11
	s_lshl_b32 s3, s2, 10
	s_ashr_i32 s47, s46, 31
	s_and_b32 s33, s3, 0x400
	s_lshl_b64 s[4:5], s[46:47], 2
	s_add_u32 s3, s26, s4
	v_lshlrev_b32_e32 v46, 2, v0
	v_mov_b32_e32 v47, 0
	s_addc_u32 s4, s27, s5
	s_lshl_b32 s5, s33, 2
	s_add_u32 s26, s3, s5
	s_addc_u32 s27, s4, 0
	v_lshlrev_b32_e32 v212, 1, v0
	v_mov_b32_e32 v213, v47
	v_lshl_add_u64 v[32:33], v[212:213], 2, s[26:27]
	v_lshrrev_b32_e32 v219, 6, v0
	v_bfe_u32 v214, v0, 5, 1
	v_and_b32_e32 v220, 31, v0
	s_or_b32 s3, s46, s33
	v_lshlrev_b32_e32 v216, 4, v219
	v_lshlrev_b32_e32 v221, 3, v214
	v_or3_b32 v1, s3, v216, v221
	v_lshlrev_b32_e32 v232, 4, v220
	v_and_b32_e32 v218, 63, v0
	s_mov_b32 s39, 0x20000
	s_brev_b32 s38, 16
	s_and_b32 s37, s37, 0xffff
	v_lshl_or_b32 v180, v1, 9, v232
	v_add_u32_e32 v1, 0x10000, v180
	global_load_dwordx2 v[32:33], v[32:33], off
	buffer_load_dwordx4 v[34:37], v180, s[36:39], 0 offen nt
	buffer_load_dwordx4 v[38:41], v180, s[36:39], 0 offen offset:512 nt
	buffer_load_dwordx4 v[42:45], v180, s[36:39], 0 offen offset:1024 nt
	buffer_load_dwordx4 v[96:99], v180, s[36:39], 0 offen offset:1536 nt
	buffer_load_dwordx4 v[100:103], v180, s[36:39], 0 offen offset:2048 nt
	buffer_load_dwordx4 v[104:107], v180, s[36:39], 0 offen offset:2560 nt
	buffer_load_dwordx4 v[108:111], v180, s[36:39], 0 offen offset:3072 nt
	buffer_load_dwordx4 v[112:115], v180, s[36:39], 0 offen offset:3584 nt
	buffer_load_dwordx4 v[116:119], v1, s[36:39], 0 offen nt
	buffer_load_dwordx4 v[120:123], v1, s[36:39], 0 offen offset:512 nt
	buffer_load_dwordx4 v[124:127], v1, s[36:39], 0 offen offset:1024 nt
	buffer_load_dwordx4 v[128:131], v1, s[36:39], 0 offen offset:1536 nt
	buffer_load_dwordx4 v[132:135], v1, s[36:39], 0 offen offset:2048 nt
	buffer_load_dwordx4 v[136:139], v1, s[36:39], 0 offen offset:2560 nt
	buffer_load_dwordx4 v[140:143], v1, s[36:39], 0 offen offset:3072 nt
	buffer_load_dwordx4 v[144:147], v1, s[36:39], 0 offen offset:3584 nt
	s_mov_b32 s3, 0x10000
	v_lshrrev_b32_e32 v227, 5, v0
	v_and_b32_e32 v228, 0x7c, v46
	v_add_u32_e32 v2, 0x200, v0
	v_lshrrev_b32_e32 v229, 5, v2
	v_mul_u32_u24_e32 v246, 0x110, v227
	v_lshl_add_u32 v246, v220, 3, v246
	v_add_u32_e32 v246, 0x10000, v246
	v_lshlrev_b32_e32 v247, 2, v46
	s_waitcnt vmcnt(16)
	v_cmp_ne_u32_e64 s[6:7], 0, v32
	v_cmp_ne_u32_e64 s[4:5], 0, v33
	v_cmp_eq_u32_e64 s[8:9], 0, v218
	s_nop 0
	s_and_saveexec_b64 s[12:13], s[8:9]
	s_cbranch_execz .LBB0_6
	s_bcnt1_i32_b64 s6, s[6:7]
	s_bcnt1_i32_b64 s4, s[4:5]
	v_mov_b32_e32 v1, 0x21100
	s_add_i32 s4, s4, s6
	v_lshl_add_u32 v1, v219, 2, v1
	v_mov_b32_e32 v2, s4
	ds_write_b32 v1, v2

	.amdhsa_kernel _Z11gram_kernelPKfPKiS0_S0_S0_S0_S0_S0_S0_S0_S0_Pf
		.amdhsa_group_segment_fixed_size 135456
		.amdhsa_private_segment_fixed_size 0
		.amdhsa_kernarg_size 96
		.amdhsa_user_sgpr_count 2
		.amdhsa_user_sgpr_dispatch_ptr 0
		.amdhsa_user_sgpr_queue_ptr 0
		.amdhsa_user_sgpr_kernarg_segment_ptr 1
		.amdhsa_user_sgpr_dispatch_id 0
		.amdhsa_user_sgpr_kernarg_preload_length 0
		.amdhsa_user_sgpr_kernarg_preload_offset 0
		.amdhsa_user_sgpr_private_segment_size 0
		.amdhsa_uses_dynamic_stack 0
		.amdhsa_enable_private_segment 0
		.amdhsa_system_sgpr_workgroup_id_x 1
		.amdhsa_system_sgpr_workgroup_id_y 0
		.amdhsa_system_sgpr_workgroup_id_z 0
		.amdhsa_system_sgpr_workgroup_info 0
		.amdhsa_system_vgpr_workitem_id 0
		.amdhsa_next_free_vgpr 250
		.amdhsa_next_free_sgpr 96
		.amdhsa_accum_offset 252
		.amdhsa_reserve_vcc 1
		.amdhsa_float_round_mode_32 0
		.amdhsa_float_round_mode_16_64 0
		.amdhsa_float_denorm_mode_32 3
		.amdhsa_float_denorm_mode_16_64 3
		.amdhsa_dx10_clamp 1
		.amdhsa_ieee_mode 1
		.amdhsa_fp16_overflow 0
		.amdhsa_tg_split 0
		.amdhsa_exception_fp_ieee_invalid_op 0
		.amdhsa_exception_fp_denorm_src 0
		.amdhsa_exception_fp_ieee_div_zero 0
		.amdhsa_exception_fp_ieee_overflow 0
		.amdhsa_exception_fp_ieee_underflow 0
		.amdhsa_exception_fp_ieee_inexact 0
		.amdhsa_exception_int_div_zero 0
	.end_amdhsa_kernel

amdhsa.kernels:
  - .agpr_count:     0
    .args:
      - .actual_access:  read_only
        .address_space:  global
        .offset:         0
        .size:           8
        .value_kind:     global_buffer
      - .actual_access:  read_only
        .address_space:  global
        .offset:         8
        .size:           8
        .value_kind:     global_buffer
      - .actual_access:  read_only
        .address_space:  global
        .offset:         16
        .size:           8
        .value_kind:     global_buffer
      - .actual_access:  read_only
        .address_space:  global
        .offset:         24
        .size:           8
        .value_kind:     global_buffer
      - .actual_access:  read_only
        .address_space:  global
        .offset:         32
        .size:           8
        .value_kind:     global_buffer
      - .actual_access:  read_only
        .address_space:  global
        .offset:         40
        .size:           8
        .value_kind:     global_buffer
      - .address_space:  global
        .offset:         48
        .size:           8
        .value_kind:     global_buffer
      - .address_space:  global
        .offset:         56
        .size:           8
        .value_kind:     global_buffer
      - .address_space:  global
        .offset:         64
        .size:           8
        .value_kind:     global_buffer
      - .actual_access:  read_only
        .address_space:  global
        .offset:         72
        .size:           8
        .value_kind:     global_buffer
      - .actual_access:  read_only
        .address_space:  global
        .offset:         80
        .size:           8
        .value_kind:     global_buffer
      - .actual_access:  write_only
        .address_space:  global
        .offset:         88
        .size:           8
        .value_kind:     global_buffer
    .group_segment_fixed_size: 135456
    .kernarg_segment_align: 8
    .kernarg_segment_size: 96
    .language:       OpenCL C
    .language_version:
      - 2
      - 0
    .max_flat_workgroup_size: 512
    .name:           _Z11gram_kernelPKfPKiS0_S0_S0_S0_S0_S0_S0_S0_S0_Pf
    .private_segment_fixed_size: 0
    .sgpr_count:     66
    .sgpr_spill_count: 0
    .symbol:         _Z11gram_kernelPKfPKiS0_S0_S0_S0_S0_S0_S0_S0_S0_Pf.kd
    .uniform_work_group_size: 1
    .uses_dynamic_stack: false
    .vgpr_count:     250
    .vgpr_spill_count: 0
    .wavefront_size: 64
  - .agpr_count:     0
    .args:
      - .actual_access:  read_only
        .address_space:  global
        .offset:         0
        .size:           8
        .value_kind:     global_buffer
      - .actual_access:  read_only
        .address_space:  global
        .offset:         8
        .size:           8
        .value_kind:     global_buffer
      - .actual_access:  write_only
        .address_space:  global
        .offset:         16
        .size:           8
        .value_kind:     global_buffer
    .group_segment_fixed_size: 0
    .kernarg_segment_align: 8
    .kernarg_segment_size: 24
    .language:       OpenCL C
    .language_version:
      - 2
      - 0
    .max_flat_workgroup_size: 256
    .name:           _Z10fin_kernelPKfS0_Pf
    .private_segment_fixed_size: 0
    .sgpr_count:     16
    .sgpr_spill_count: 0
    .symbol:         _Z10fin_kernelPKfS0_Pf.kd
    .uniform_work_group_size: 1
    .uses_dynamic_stack: false
    .vgpr_count:     51
    .vgpr_spill_count: 0
    .wavefront_size: 64
